# sc1 write-through also on k_prep and k_mid stores
# baseline (speedup 1.0000x reference)
.LBB0_3:
	s_cmpk_gt_u32 s2, 0xdff
	s_cbranch_scc0 .LBB0_13
	s_cmpk_gt_u32 s2, 0x11ff
	s_cbranch_scc0 .LBB0_6
	s_load_dwordx8 s[4:11], s[0:1], 0x10
	s_load_dwordx2 s[14:15], s[0:1], 0x30
	v_lshl_or_b32 v1, s2, 8, v0
	v_add_u32_e32 v2, 0xffee0000, v1
	v_mov_b32_e32 v3, 0
	v_lshlrev_b64 v[4:5], 2, v[2:3]
	s_waitcnt lgkmcnt(0)
	v_lshl_add_u64 v[6:7], s[6:7], 0, v[4:5]
	global_load_dword v22, v[6:7], off
	v_lshl_add_u64 v[6:7], s[10:11], 0, v[4:5]
	global_load_dword v23, v[6:7], off
	v_lshl_add_u64 v[6:7], s[4:5], 0, v[4:5]
	global_load_dword v24, v[6:7], off
	v_lshl_add_u64 v[6:7], s[8:9], 0, v[4:5]
	global_load_dword v25, v[6:7], off
	v_add_u32_e32 v6, 0xffee0800, v1
	v_mov_b32_e32 v7, v3
	v_lshlrev_b64 v[6:7], 2, v[6:7]
	v_lshl_add_u64 v[8:9], s[4:5], 0, v[6:7]
	global_load_dword v1, v[8:9], off
	v_lshl_add_u64 v[8:9], s[14:15], 0, v[4:5]
	global_load_dword v26, v[8:9], off
	s_add_u32 s4, s12, 0xd000000
	s_mov_b32 s3, 0xd002000
	s_addc_u32 s5, s13, 0
	v_lshl_add_u64 v[12:13], s[12:13], 0, v[4:5]
	s_add_u32 s6, s12, 0xd004000
	v_ashrrev_i32_e32 v9, 31, v2
	v_mov_b32_e32 v8, v2
	v_add_co_u32_e32 v12, vcc, s3, v12
	s_mov_b32 s8, 0x5c000
	s_addc_u32 s7, s13, 0
	v_lshl_add_u64 v[8:9], v[8:9], 2, s[4:5]
	v_addc_co_u32_e32 v13, vcc, 0, v13, vcc
	v_mov_b32_e32 v19, 0x3a4ccccd
	v_lshl_add_u64 v[16:17], s[6:7], 0, v[6:7]
	v_add_co_u32_e32 v18, vcc, s8, v8
	s_mov_b32 s9, 0x1a000
	global_store_dword v[16:17], v19, off sc1
	v_addc_co_u32_e32 v19, vcc, 0, v9, vcc
	v_add_co_u32_e32 v16, vcc, s9, v8
	v_lshl_add_u64 v[10:11], s[4:5], 0, v[4:5]
	s_add_u32 s4, s12, 0xd008000
	v_addc_co_u32_e32 v17, vcc, 0, v9, vcc
	s_addc_u32 s5, s13, 0
	v_add_co_u32_e32 v20, vcc, 0xc000, v8
	v_lshl_add_u64 v[6:7], s[4:5], 0, v[6:7]
	s_nop 0
	v_addc_co_u32_e32 v21, vcc, 0, v9, vcc
	global_store_dword v[6:7], v3, off sc1
	global_store_dword v[18:19], v3, off sc1
	global_store_dword v[16:17], v3, off sc1
	v_add_co_u32_e32 v6, vcc, 0xe000, v8
	v_lshl_add_u64 v[14:15], s[6:7], 0, v[4:5]
	s_nop 0
	v_addc_co_u32_e32 v7, vcc, 0, v9, vcc
	v_lshl_add_u64 v[4:5], s[4:5], 0, v[4:5]
	global_store_dword v[20:21], v3, off sc1
	global_store_dword v[6:7], v3, off sc1
	s_mov_b64 s[4:5], 0
	s_waitcnt vmcnt(11)
	v_mul_f32_e32 v2, 0x3a4ccccd, v22
	s_waitcnt vmcnt(10)
	v_mul_f32_e32 v3, 0x3a4ccccd, v23
	s_waitcnt vmcnt(8)
	v_fmac_f32_e32 v25, v22, v24
	s_waitcnt vmcnt(6)
	v_fmac_f32_e32 v26, v23, v1
	global_store_dword v[10:11], v2, off sc1
	global_store_dword v[12:13], v25, off sc1
	global_store_dword v[14:15], v3, off sc1
	global_store_dword v[4:5], v26, off sc1
.LBB0_6:
	s_andn2_b64 vcc, exec, s[4:5]
	s_cbranch_vccnz .LBB0_12
	s_load_dwordx2 s[6:7], s[0:1], 0x38
	s_add_i32 s3, s2, 0xfffff200
	s_lshr_b32 s4, s3, 5
	s_lshl_b32 s3, s2, 6
	s_and_b32 s3, s3, 0x7c0
	s_lshl_b32 s5, s4, 6
	s_lshl_b32 s8, s3, 2
	v_lshrrev_b32_e32 v1, 4, v0
	s_waitcnt lgkmcnt(0)
	s_add_u32 s6, s6, s8
	v_lshlrev_b32_e32 v2, 4, v0
	s_addc_u32 s7, s7, 0
	v_and_b32_e32 v2, 0xf0, v2
	v_mov_b32_e32 v3, 0
	v_or_b32_e32 v4, s5, v1
	v_lshl_add_u64 v[16:17], s[6:7], 0, v[2:3]
	v_lshlrev_b32_e32 v18, 11, v4
	v_mov_b32_e32 v19, v3
	s_movk_i32 s10, 0x104
	v_lshl_add_u64 v[12:13], v[18:19], 2, v[16:17]
	v_mad_u32_u24 v1, v1, s10, v2
	v_or_b32_e32 v2, 0x8000, v18
	v_lshl_add_u64 v[14:15], v[2:3], 2, v[16:17]
	global_load_dwordx4 v[4:7], v[12:13], off nt
	global_load_dwordx4 v[8:11], v[14:15], off nt
	v_or_b32_e32 v2, 0x10000, v18
	v_lshl_add_u64 v[12:13], v[2:3], 2, v[16:17]
	global_load_dwordx4 v[12:15], v[12:13], off nt
	v_or_b32_e32 v2, 0x18000, v18
	v_lshl_add_u64 v[16:17], v[2:3], 2, v[16:17]
	global_load_dwordx4 v[16:19], v[16:17], off nt
	v_lshrrev_b32_e32 v2, 3, v0
	v_lshlrev_b32_e32 v20, 3, v0
	v_lshlrev_b32_e32 v22, 2, v2
	v_or_b32_e32 v23, s3, v2
	v_and_b32_e32 v2, 56, v20
	v_mad_u32_u24 v31, v2, s10, v22
	v_add_u32_e32 v24, 0x1040, v1
	v_add_u32_e32 v25, 0x1048, v1
	v_add_u32_e32 v27, 0x2080, v1
	v_add_u32_e32 v28, 0x2088, v1
	v_add_u32_e32 v29, 0x30c0, v1
	v_add_u32_e32 v30, 0x30c8, v1
	v_add_u32_e32 v32, 0x400, v31
	s_mov_b32 s11, 0xc3e00000
	v_mov_b32_e32 v26, 0x43e00000
	s_add_u32 s8, s12, s5
	s_addc_u32 s9, s13, 0
	s_mov_b64 s[6:7], 0x4000000
	v_lshl_add_u64 v[20:21], s[8:9], 0, v[2:3]
	v_lshlrev_b32_e32 v2, 11, v23
	v_lshl_add_u64 v[20:21], v[20:21], 0, s[6:7]
	v_lshl_add_u64 v[22:23], v[20:21], 0, v[2:3]
	v_or_b32_e32 v2, 0x10000, v2
	s_mov_b32 s5, 0
	v_cmp_gt_u32_e32 vcc, 64, v0
	s_waitcnt vmcnt(3)
	ds_write2_b32 v1, v4, v5 offset1:1
	ds_write2_b32 v1, v6, v7 offset0:2 offset1:3
	s_waitcnt vmcnt(2)
	ds_write2_b32 v24, v8, v9 offset1:1
	ds_write2_b32 v25, v10, v11 offset1:1
	s_waitcnt vmcnt(1)
	ds_write2_b32 v27, v12, v13 offset1:1
	ds_write2_b32 v28, v14, v15 offset1:1
	s_waitcnt vmcnt(0)
	ds_write2_b32 v29, v16, v17 offset1:1
	ds_write2_b32 v30, v18, v19 offset1:1
	s_waitcnt lgkmcnt(0)
	s_barrier
	ds_read2_b32 v[4:5], v31 offset1:65
	ds_read2_b32 v[6:7], v31 offset0:130 offset1:195
	ds_read2_b32 v[8:9], v32 offset0:4 offset1:69
	ds_read2_b32 v[10:11], v32 offset0:134 offset1:199
	s_waitcnt lgkmcnt(3)
	v_mul_f32_e32 v1, 0x42800000, v4
	v_mul_f32_e32 v4, 0x42800000, v5
	s_waitcnt lgkmcnt(2)
	v_mul_f32_e32 v5, 0x42800000, v6
	v_mul_f32_e32 v6, 0x42800000, v7
	s_waitcnt lgkmcnt(1)
	v_mul_f32_e32 v7, 0x42800000, v8
	v_mul_f32_e32 v8, 0x42800000, v9
	v_med3_f32 v1, v1, s11, v26
	v_med3_f32 v4, v4, s11, v26
	v_med3_f32 v7, v7, s11, v26
	v_med3_f32 v8, v8, s11, v26
	v_cvt_pk_fp8_f32 v12, v1, v4
	v_cvt_pk_fp8_f32 v13, v7, v8
	s_waitcnt lgkmcnt(0)
	v_mul_f32_e32 v9, 0x42800000, v10
	v_mul_f32_e32 v10, 0x42800000, v11
	v_med3_f32 v5, v5, s11, v26
	v_med3_f32 v6, v6, s11, v26
	v_med3_f32 v1, v9, s11, v26
	v_med3_f32 v4, v10, s11, v26
	ds_read2_b32 v[14:15], v31 offset0:32 offset1:97
	ds_read2_b32 v[16:17], v31 offset0:162 offset1:227
	ds_read2_b32 v[18:19], v32 offset0:36 offset1:101
	ds_read2_b32 v[24:25], v32 offset0:166 offset1:231
	v_cvt_pk_fp8_f32 v12, v5, v6 op_sel:[0,0,1]
	v_cvt_pk_fp8_f32 v13, v1, v4 op_sel:[0,0,1]
	s_waitcnt lgkmcnt(3)
	v_mul_f32_e32 v11, 0x42800000, v14
	v_mul_f32_e32 v14, 0x42800000, v15
	s_waitcnt lgkmcnt(2)
	v_mul_f32_e32 v15, 0x42800000, v16
	v_mul_f32_e32 v16, 0x42800000, v17
	s_waitcnt lgkmcnt(1)
	v_mul_f32_e32 v17, 0x42800000, v18
	v_mul_f32_e32 v18, 0x42800000, v19
	v_med3_f32 v1, v11, s11, v26
	v_med3_f32 v5, v14, s11, v26
	global_store_dwordx2 v[22:23], v[12:13], off sc1
	v_med3_f32 v7, v17, s11, v26
	v_cvt_pk_fp8_f32 v4, v1, v5
	v_med3_f32 v8, v18, s11, v26
	v_cvt_pk_fp8_f32 v5, v7, v8
	s_waitcnt lgkmcnt(0)
	v_mul_f32_e32 v19, 0x42800000, v24
	v_mul_f32_e32 v24, 0x42800000, v25
	v_med3_f32 v6, v15, s11, v26
	v_med3_f32 v1, v16, s11, v26
	v_cvt_pk_fp8_f32 v4, v6, v1 op_sel:[0,0,1]
	v_med3_f32 v1, v19, s11, v26
	v_med3_f32 v6, v24, s11, v26
	v_cvt_pk_fp8_f32 v5, v1, v6 op_sel:[0,0,1]
	v_lshl_add_u64 v[6:7], v[20:21], 0, v[2:3]
	global_store_dwordx2 v[6:7], v[4:5], off sc1
	s_and_saveexec_b64 s[6:7], vcc
	s_cbranch_execz .LBB0_11
	v_lshlrev_b32_e32 v1, 2, v0
.LBB0_9:
	v_add_u32_e32 v2, s5, v1
	ds_read2_b32 v[4:5], v2 offset1:65
	ds_read2_b32 v[6:7], v2 offset0:130 offset1:195
	v_add_u32_e32 v2, 0x400, v2
	ds_read2_b32 v[8:9], v2 offset0:4 offset1:69
	ds_read2_b32 v[10:11], v2 offset0:134 offset1:199
	s_addk_i32 s5, 0x820
	s_waitcnt lgkmcnt(3)
	v_add_f32_e32 v2, v3, v4
	v_add_f32_e32 v2, v2, v5
	s_waitcnt lgkmcnt(2)
	v_add_f32_e32 v2, v2, v6
	v_add_f32_e32 v2, v2, v7
	s_waitcnt lgkmcnt(1)
	v_add_f32_e32 v2, v2, v8
	v_add_f32_e32 v2, v2, v9
	s_waitcnt lgkmcnt(0)
	v_add_f32_e32 v2, v2, v10
	s_cmpk_eq_i32 s5, 0x4100
	v_add_f32_e32 v3, v2, v11
	s_cbranch_scc0 .LBB0_9
	s_mov_b32 s5, 0
	s_lshl_b64 s[4:5], s[4:5], 13
	s_add_u32 s4, s12, s4
	v_or_b32_e32 v1, s3, v0
	s_addc_u32 s5, s13, s5
	v_lshlrev_b32_e32 v4, 2, v1
	v_mov_b32_e32 v5, 0
	v_lshl_add_u64 v[4:5], s[4:5], 0, v[4:5]
	v_add_co_u32_e32 v4, vcc, 0xd01c000, v4
	s_nop 1
	v_addc_co_u32_e32 v5, vcc, 0, v5, vcc
	global_store_dword v[4:5], v3, off sc1

.LBB0_13:
	s_andn2_b64 vcc, exec, s[4:5]
	s_cbranch_vccnz .LBB0_15
	s_add_i32 s3, s2, 0xfe00
	s_and_b32 s6, s3, 0xffff
	s_mul_i32 s6, s6, 0xaaab
	s_lshr_b32 s7, s6, 16
	s_lshr_b32 s6, s6, 22
	s_load_dwordx2 s[4:5], s[0:1], 0x8
	s_mulk_i32 s6, 0x60
	s_sub_i32 s3, s3, s6
	s_lshl_b32 s3, s3, 6
	s_and_b32 s3, s3, 0xffc0
	s_lshl_b32 s6, s3, 2
	s_waitcnt lgkmcnt(0)
	s_add_u32 s4, s4, s6
	v_lshrrev_b32_e32 v1, 4, v0
	s_addc_u32 s5, s5, 0
	s_and_b32 s6, s7, 0xffc0
	v_lshlrev_b32_e32 v2, 4, v0
	v_or_b32_e32 v16, s6, v1
	v_and_b32_e32 v18, 0xf0, v2
	v_mov_b32_e32 v19, 0
	v_mul_u32_u24_e32 v2, 0x1800, v16
	v_lshl_add_u64 v[14:15], s[4:5], 0, v[18:19]
	v_lshlrev_b32_e32 v2, 2, v2
	v_mov_b32_e32 v3, v19
	v_lshl_add_u64 v[10:11], v[14:15], 0, v[2:3]
	v_or_b32_e32 v2, 16, v16
	s_movk_i32 s8, 0x104
	v_mul_u32_u24_e32 v2, 0x1800, v2
	v_mad_u32_u24 v1, v1, s8, v18
	v_lshlrev_b32_e32 v18, 2, v2
	v_lshl_add_u64 v[12:13], v[14:15], 0, v[18:19]
	global_load_dwordx4 v[2:5], v[10:11], off nt
	global_load_dwordx4 v[6:9], v[12:13], off nt
	v_or_b32_e32 v10, 32, v16
	v_mul_u32_u24_e32 v10, 0x1800, v10
	v_lshlrev_b32_e32 v18, 2, v10
	v_or_b32_e32 v16, 48, v16
	v_lshl_add_u64 v[10:11], v[14:15], 0, v[18:19]
	v_mul_u32_u24_e32 v16, 0x1800, v16
	global_load_dwordx4 v[10:13], v[10:11], off nt
	v_lshlrev_b32_e32 v18, 2, v16
	v_lshl_add_u64 v[14:15], v[14:15], 0, v[18:19]
	global_load_dwordx4 v[14:17], v[14:15], off nt
	v_lshrrev_b32_e32 v24, 3, v0
	v_lshlrev_b32_e32 v18, 3, v0
	s_add_u32 s6, s12, s6
	v_lshlrev_b32_e32 v22, 2, v24
	s_addc_u32 s7, s13, 0
	v_and_b32_e32 v18, 56, v18
	v_lshl_add_u64 v[20:21], s[6:7], 0, v[18:19]
	v_mad_u32_u24 v18, v18, s8, v22
	v_add_u32_e32 v23, 0x1040, v1
	v_add_u32_e32 v25, 0x1048, v1
	v_add_u32_e32 v27, 0x2080, v1
	v_add_u32_e32 v28, 0x2088, v1
	v_add_u32_e32 v29, 0x30c0, v1
	v_add_u32_e32 v30, 0x30c8, v1
	v_add_u32_e32 v22, 0x400, v18
	s_mov_b32 s9, 0xc2fe0000
	v_mov_b32_e32 v26, 0x42fe0000
	s_mov_b32 s10, 0x40c0c00
	s_mov_b64 s[4:5], 0x2000000
	v_lshl_add_u64 v[20:21], v[20:21], 0, s[4:5]
	s_waitcnt vmcnt(3)
	ds_write2_b32 v1, v2, v3 offset1:1
	ds_write2_b32 v1, v4, v5 offset0:2 offset1:3
	s_waitcnt vmcnt(2)
	ds_write2_b32 v23, v6, v7 offset1:1
	ds_write2_b32 v25, v8, v9 offset1:1
	s_waitcnt vmcnt(1)
	ds_write2_b32 v27, v10, v11 offset1:1
	ds_write2_b32 v28, v12, v13 offset1:1
	s_waitcnt vmcnt(0)
	ds_write2_b32 v29, v14, v15 offset1:1
	ds_write2_b32 v30, v16, v17 offset1:1
	s_waitcnt lgkmcnt(0)
	s_barrier
	ds_read2_b32 v[2:3], v18 offset1:32
	ds_read2_b32 v[4:5], v18 offset0:65 offset1:97
	ds_read2_b32 v[6:7], v18 offset0:130 offset1:162
	ds_read2_b32 v[8:9], v18 offset0:195 offset1:227
	ds_read2_b32 v[10:11], v22 offset0:4 offset1:36
	ds_read2_b32 v[12:13], v22 offset0:69 offset1:101
	ds_read2_b32 v[14:15], v22 offset0:134 offset1:166
	ds_read2_b32 v[16:17], v22 offset0:199 offset1:231
	s_waitcnt lgkmcnt(7)
	v_mul_f32_e32 v1, 0x44a00000, v2
	s_waitcnt lgkmcnt(6)
	v_mul_f32_e32 v2, 0x44a00000, v4
	s_waitcnt lgkmcnt(5)
	v_mul_f32_e32 v4, 0x44a00000, v6
	s_waitcnt lgkmcnt(4)
	v_mul_f32_e32 v6, 0x44a00000, v8
	v_med3_f32 v2, v2, s9, v26
	v_med3_f32 v1, v1, s9, v26
	v_med3_f32 v4, v4, s9, v26
	v_med3_f32 v6, v6, s9, v26
	v_rndne_f32_e32 v2, v2
	v_rndne_f32_e32 v1, v1
	v_rndne_f32_e32 v4, v4
	v_rndne_f32_e32 v6, v6
	v_cvt_i32_f32_e32 v2, v2
	v_cvt_i32_f32_e32 v1, v1
	v_cvt_i32_f32_sdwa v4, v4 dst_sel:WORD_1 dst_unused:UNUSED_PAD src0_sel:DWORD
	v_cvt_i32_f32_e32 v6, v6
	s_waitcnt lgkmcnt(3)
	v_mul_f32_e32 v8, 0x44a00000, v10
	s_waitcnt lgkmcnt(2)
	v_mul_f32_e32 v10, 0x44a00000, v12
	v_lshlrev_b32_e32 v2, 8, v2
	s_waitcnt lgkmcnt(1)
	v_mul_f32_e32 v12, 0x44a00000, v14
	s_waitcnt lgkmcnt(0)
	v_mul_f32_e32 v14, 0x44a00000, v16
	v_med3_f32 v10, v10, s9, v26
	v_and_b32_e32 v4, 0xff0000, v4
	v_perm_b32 v1, v6, v1, s10
	v_and_b32_e32 v2, 0xff00, v2
	v_med3_f32 v8, v8, s9, v26
	v_rndne_f32_e32 v10, v10
	v_or3_b32 v22, v1, v2, v4
	v_med3_f32 v1, v12, s9, v26
	v_med3_f32 v2, v14, s9, v26
	v_rndne_f32_e32 v8, v8
	v_cvt_i32_f32_e32 v10, v10
	v_rndne_f32_e32 v1, v1
	v_rndne_f32_e32 v2, v2
	v_cvt_i32_f32_e32 v8, v8
	v_cvt_i32_f32_sdwa v1, v1 dst_sel:WORD_1 dst_unused:UNUSED_PAD src0_sel:DWORD
	v_cvt_i32_f32_e32 v2, v2
	v_lshlrev_b32_e32 v4, 8, v10
	v_and_b32_e32 v4, 0xff00, v4
	v_and_b32_e32 v1, 0xff0000, v1
	v_perm_b32 v2, v2, v8, s10
	v_or3_b32 v23, v2, v4, v1
	v_or_b32_e32 v1, s3, v24
	v_mul_f32_e32 v2, 0x44a00000, v5
	v_lshlrev_b32_e32 v18, 11, v1
	v_mul_f32_e32 v1, 0x44a00000, v3
	v_mul_f32_e32 v3, 0x44a00000, v7
	v_mul_f32_e32 v4, 0x44a00000, v9
	v_med3_f32 v2, v2, s9, v26
	v_med3_f32 v1, v1, s9, v26
	v_rndne_f32_e32 v2, v2
	v_med3_f32 v3, v3, s9, v26
	v_med3_f32 v4, v4, s9, v26
	v_rndne_f32_e32 v1, v1
	v_cvt_i32_f32_e32 v2, v2
	v_rndne_f32_e32 v3, v3
	v_rndne_f32_e32 v4, v4
	v_cvt_i32_f32_e32 v1, v1
	v_cvt_i32_f32_sdwa v3, v3 dst_sel:WORD_1 dst_unused:UNUSED_PAD src0_sel:DWORD
	v_cvt_i32_f32_e32 v4, v4
	v_lshlrev_b32_e32 v2, 8, v2
	v_mul_f32_e32 v6, 0x44a00000, v13
	v_and_b32_e32 v2, 0xff00, v2
	v_and_b32_e32 v3, 0xff0000, v3
	v_perm_b32 v1, v4, v1, s10
	v_mul_f32_e32 v5, 0x44a00000, v11
	v_mul_f32_e32 v7, 0x44a00000, v15
	v_mul_f32_e32 v8, 0x44a00000, v17
	v_or3_b32 v2, v1, v2, v3
	v_med3_f32 v3, v6, s9, v26
	v_med3_f32 v1, v5, s9, v26
	v_rndne_f32_e32 v3, v3
	v_med3_f32 v4, v7, s9, v26
	v_med3_f32 v5, v8, s9, v26
	v_rndne_f32_e32 v1, v1
	v_cvt_i32_f32_e32 v3, v3
	v_rndne_f32_e32 v4, v4
	v_rndne_f32_e32 v5, v5
	v_cvt_i32_f32_e32 v1, v1
	v_cvt_i32_f32_sdwa v4, v4 dst_sel:WORD_1 dst_unused:UNUSED_PAD src0_sel:DWORD
	v_cvt_i32_f32_e32 v5, v5
	v_lshlrev_b32_e32 v3, 8, v3
	v_lshl_add_u64 v[24:25], v[20:21], 0, v[18:19]
	v_and_b32_e32 v3, 0xff00, v3
	v_and_b32_e32 v4, 0xff0000, v4
	v_perm_b32 v1, v5, v1, s10
	v_or_b32_e32 v18, 0x10000, v18
	v_or3_b32 v3, v1, v3, v4
	v_lshl_add_u64 v[4:5], v[20:21], 0, v[18:19]
	global_store_dwordx2 v[24:25], v[22:23], off sc1
	global_store_dwordx2 v[4:5], v[2:3], off sc1

.LBB0_18:
	v_lshl_add_u64 v[34:35], v[68:69], 0, s[4:5]
	global_load_dwordx4 v[62:65], v[34:35], off nt
	global_load_dwordx4 v[58:61], v[34:35], off offset:1024 nt
	global_load_dwordx4 v[54:57], v[34:35], off offset:2048 nt
	global_load_dwordx4 v[50:53], v[34:35], off offset:3072 nt
	v_add_co_u32_e32 v80, vcc, s3, v34
	s_waitcnt vmcnt(2)
	v_max_f32_e64 v82, |v61|, |v61|
	v_addc_co_u32_e32 v81, vcc, 0, v35, vcc
	global_load_dwordx4 v[46:49], v[80:81], off nt
	global_load_dwordx4 v[42:45], v[80:81], off offset:1024 nt
	global_load_dwordx4 v[38:41], v[80:81], off offset:2048 nt
	global_load_dwordx4 v[34:37], v[80:81], off offset:3072 nt
	v_max_f32_e64 v80, |v65|, |v65|
	v_max_f32_e64 v81, |v64|, |v64|
	v_max_f32_e64 v83, |v60|, |v60|
	s_waitcnt vmcnt(5)
	v_max_f32_e64 v84, |v57|, |v57|
	v_max_f32_e64 v85, |v56|, |v56|
	s_waitcnt vmcnt(4)
	v_max_f32_e64 v86, |v53|, |v53|
	v_max_f32_e64 v87, |v52|, |v52|
	v_max_f32_e32 v80, v81, v80
	v_max_f32_e32 v81, v83, v82
	v_max_f32_e32 v82, v85, v84
	v_max_f32_e32 v83, v87, v86
	v_max3_f32 v80, |v62|, |v63|, v80
	v_max3_f32 v81, |v58|, |v59|, v81
	v_max3_f32 v82, |v54|, |v55|, v82
	v_max3_f32 v83, |v50|, |v51|, v83
	v_max3_f32 v80, v80, 0, v81
	v_max3_f32 v80, v80, v82, v83
	v_lshl_add_u64 v[82:83], s[12:13], 0, v[70:71]
	s_waitcnt vmcnt(3)
	v_max_f32_e64 v84, |v49|, |v49|
	v_max_f32_e64 v85, |v48|, |v48|
	s_waitcnt vmcnt(2)
	v_max_f32_e64 v86, |v45|, |v45|
	v_max_f32_e64 v87, |v44|, |v44|
	s_waitcnt vmcnt(1)
	v_max_f32_e64 v88, |v41|, |v41|
	v_max_f32_e64 v89, |v40|, |v40|
	s_waitcnt vmcnt(0)
	v_max_f32_e64 v90, |v37|, |v37|
	v_max_f32_e64 v91, |v36|, |v36|
	v_max_f32_e32 v84, v85, v84
	v_max_f32_e32 v85, v87, v86
	v_max_f32_e32 v86, v89, v88
	v_max_f32_e32 v87, v91, v90
	v_max3_f32 v81, |v46|, |v47|, v84
	v_max3_f32 v84, |v42|, |v43|, v85
	v_max3_f32 v85, |v38|, |v39|, v86
	v_max3_f32 v86, |v34|, |v35|, v87
	v_max3_f32 v80, v80, v81, v84
	v_max3_f32 v80, v80, v85, v86
	ds_bpermute_b32 v81, v73, v80
	s_waitcnt lgkmcnt(0)
	v_max_f32_e32 v81, v81, v81
	v_max_f32_e32 v80, v80, v81
	ds_bpermute_b32 v81, v74, v80
	s_waitcnt lgkmcnt(0)
	v_max_f32_e32 v81, v81, v81
	v_max_f32_e32 v80, v80, v81
	ds_bpermute_b32 v81, v75, v80
	s_waitcnt lgkmcnt(0)
	v_max_f32_e32 v81, v81, v81
	v_max_f32_e32 v80, v80, v81
	ds_bpermute_b32 v81, v76, v80
	s_waitcnt lgkmcnt(0)
	v_max_f32_e32 v81, v81, v81
	v_max_f32_e32 v80, v80, v81
	ds_bpermute_b32 v81, v77, v80
	s_waitcnt lgkmcnt(0)
	v_max_f32_e32 v81, v81, v81
	v_max_f32_e32 v80, v80, v81
	ds_bpermute_b32 v81, v78, v80
	s_waitcnt lgkmcnt(0)
	v_max3_f32 v80, v80, v81, s10
	v_div_scale_f32 v81, s[8:9], v80, v80, s11
	v_rcp_f32_e32 v84, v81
	v_div_scale_f32 v85, vcc, s11, v80, s11
	v_fma_f32 v86, -v81, v84, 1.0
	v_fmac_f32_e32 v84, v86, v84
	v_mul_f32_e32 v86, v85, v84
	v_fma_f32 v87, -v81, v86, v85
	v_fmac_f32_e32 v86, v87, v84
	v_fma_f32 v81, -v81, v86, v85
	v_div_fmas_f32 v81, v81, v84, v86
	v_div_fixup_f32 v81, v81, v80, s11
	v_mul_f32_e32 v84, v81, v62
	v_mul_f32_e32 v85, v81, v63
	v_mul_f32_e32 v87, v81, v65
	v_mul_f32_e32 v89, v81, v59
	v_mul_f32_e32 v86, v81, v64
	v_mul_f32_e32 v88, v81, v58
	v_mul_f32_e32 v90, v81, v60
	v_mul_f32_e32 v91, v81, v61
	v_mul_f32_e32 v93, v81, v55
	v_med3_f32 v84, v84, s14, v79
	v_med3_f32 v85, v85, s14, v79
	v_med3_f32 v87, v87, s14, v79
	v_med3_f32 v89, v89, s14, v79
	v_mul_f32_e32 v92, v81, v54
	v_mul_f32_e32 v94, v81, v56
	v_mul_f32_e32 v95, v81, v57
	v_med3_f32 v86, v86, s14, v79
	v_med3_f32 v88, v88, s14, v79
	v_med3_f32 v90, v90, s14, v79
	v_med3_f32 v91, v91, s14, v79
	v_med3_f32 v93, v93, s14, v79
	v_rndne_f32_e32 v84, v84
	v_rndne_f32_e32 v85, v85
	v_rndne_f32_e32 v87, v87
	v_rndne_f32_e32 v89, v89
	v_med3_f32 v92, v92, s14, v79
	v_med3_f32 v94, v94, s14, v79
	v_med3_f32 v95, v95, s14, v79
	v_rndne_f32_e32 v86, v86
	v_rndne_f32_e32 v88, v88
	v_rndne_f32_e32 v90, v90
	v_rndne_f32_e32 v91, v91
	v_rndne_f32_e32 v93, v93
	v_cvt_i32_f32_e32 v84, v84
	v_cvt_i32_f32_e32 v85, v85
	v_cvt_i32_f32_e32 v87, v87
	v_cvt_i32_f32_e32 v89, v89
	v_rndne_f32_e32 v92, v92
	v_rndne_f32_e32 v94, v94
	v_rndne_f32_e32 v95, v95
	v_cvt_i32_f32_sdwa v86, v86 dst_sel:WORD_1 dst_unused:UNUSED_PAD src0_sel:DWORD
	v_cvt_i32_f32_e32 v88, v88
	v_cvt_i32_f32_sdwa v90, v90 dst_sel:WORD_1 dst_unused:UNUSED_PAD src0_sel:DWORD
	v_cvt_i32_f32_e32 v91, v91
	v_cvt_i32_f32_e32 v93, v93
	v_cvt_i32_f32_e32 v92, v92
	v_cvt_i32_f32_sdwa v94, v94 dst_sel:WORD_1 dst_unused:UNUSED_PAD src0_sel:DWORD
	v_cvt_i32_f32_e32 v95, v95
	v_lshlrev_b32_e32 v85, 8, v85
	v_perm_b32 v84, v87, v84, s15
	v_lshlrev_b32_e32 v87, 8, v89
	v_and_b32_e32 v86, 0xff0000, v86
	v_and_b32_e32 v89, 0xff0000, v90
	v_perm_b32 v88, v91, v88, s15
	v_lshlrev_b32_e32 v90, 8, v93
	v_and_b32_e32 v85, 0xff00, v85
	v_and_b32_e32 v87, 0xff00, v87
	v_mul_f32_e32 v97, v81, v51
	v_and_b32_e32 v91, 0xff0000, v94
	v_perm_b32 v92, v95, v92, s15
	v_and_b32_e32 v90, 0xff00, v90
	v_or3_b32 v84, v84, v85, v86
	v_or3_b32 v85, v88, v87, v89
	v_mul_f32_e32 v96, v81, v50
	v_mul_f32_e32 v98, v81, v52
	v_mul_f32_e32 v99, v81, v53
	v_or3_b32 v86, v92, v90, v91
	global_store_dword v[82:83], v84, off sc1
	global_store_dword v[82:83], v85, off offset:256 sc1
	global_store_dword v[82:83], v86, off offset:512 sc1
	v_med3_f32 v85, v97, s14, v79
	v_med3_f32 v96, v96, s14, v79
	v_rndne_f32_e32 v85, v85
	v_med3_f32 v86, v98, s14, v79
	v_med3_f32 v87, v99, s14, v79
	v_rndne_f32_e32 v96, v96
	v_cvt_i32_f32_e32 v85, v85
	v_rndne_f32_e32 v86, v86
	v_rndne_f32_e32 v87, v87
	v_cvt_i32_f32_e32 v84, v96
	v_cvt_i32_f32_sdwa v86, v86 dst_sel:WORD_1 dst_unused:UNUSED_PAD src0_sel:DWORD
	v_cvt_i32_f32_e32 v87, v87
	v_lshlrev_b32_e32 v85, 8, v85
	v_and_b32_e32 v85, 0xff00, v85
	v_and_b32_e32 v86, 0xff0000, v86
	v_perm_b32 v84, v87, v84, s15
	v_or3_b32 v84, v84, v85, v86
	v_mul_f32_e32 v85, v81, v47
	global_store_dword v[82:83], v84, off offset:768 sc1
	v_mul_f32_e32 v84, v81, v46
	v_mul_f32_e32 v86, v81, v48
	v_mul_f32_e32 v87, v81, v49
	v_med3_f32 v85, v85, s14, v79
	v_med3_f32 v84, v84, s14, v79
	v_rndne_f32_e32 v85, v85
	v_med3_f32 v86, v86, s14, v79
	v_med3_f32 v87, v87, s14, v79
	v_rndne_f32_e32 v84, v84
	v_cvt_i32_f32_e32 v85, v85
	v_rndne_f32_e32 v86, v86
	v_rndne_f32_e32 v87, v87
	v_cvt_i32_f32_e32 v84, v84
	v_cvt_i32_f32_sdwa v86, v86 dst_sel:WORD_1 dst_unused:UNUSED_PAD src0_sel:DWORD
	v_cvt_i32_f32_e32 v87, v87
	v_lshlrev_b32_e32 v85, 8, v85
	v_and_b32_e32 v85, 0xff00, v85
	v_and_b32_e32 v86, 0xff0000, v86
	v_perm_b32 v84, v87, v84, s15
	v_or3_b32 v84, v84, v85, v86
	v_mul_f32_e32 v85, v81, v43
	global_store_dword v[82:83], v84, off offset:1024 sc1
	v_mul_f32_e32 v84, v81, v42
	v_mul_f32_e32 v86, v81, v44
	v_mul_f32_e32 v87, v81, v45
	v_med3_f32 v85, v85, s14, v79
	v_med3_f32 v84, v84, s14, v79
	v_rndne_f32_e32 v85, v85
	v_med3_f32 v86, v86, s14, v79
	v_med3_f32 v87, v87, s14, v79
	v_rndne_f32_e32 v84, v84
	v_cvt_i32_f32_e32 v85, v85
	v_rndne_f32_e32 v86, v86
	v_rndne_f32_e32 v87, v87
	v_cvt_i32_f32_e32 v84, v84
	v_cvt_i32_f32_sdwa v86, v86 dst_sel:WORD_1 dst_unused:UNUSED_PAD src0_sel:DWORD
	v_cvt_i32_f32_e32 v87, v87
	v_lshlrev_b32_e32 v85, 8, v85
	v_and_b32_e32 v85, 0xff00, v85
	v_and_b32_e32 v86, 0xff0000, v86
	v_perm_b32 v84, v87, v84, s15
	v_or3_b32 v84, v84, v85, v86
	v_mul_f32_e32 v85, v81, v39
	global_store_dword v[82:83], v84, off offset:1280 sc1
	v_mul_f32_e32 v84, v81, v38
	v_mul_f32_e32 v86, v81, v40
	v_mul_f32_e32 v87, v81, v41
	v_med3_f32 v85, v85, s14, v79
	v_med3_f32 v84, v84, s14, v79
	v_rndne_f32_e32 v85, v85
	v_med3_f32 v86, v86, s14, v79
	v_med3_f32 v87, v87, s14, v79
	v_rndne_f32_e32 v84, v84
	v_cvt_i32_f32_e32 v85, v85
	v_rndne_f32_e32 v86, v86
	v_rndne_f32_e32 v87, v87
	v_cvt_i32_f32_e32 v84, v84
	v_cvt_i32_f32_sdwa v86, v86 dst_sel:WORD_1 dst_unused:UNUSED_PAD src0_sel:DWORD
	v_cvt_i32_f32_e32 v87, v87
	v_lshlrev_b32_e32 v85, 8, v85
	v_and_b32_e32 v85, 0xff00, v85
	v_and_b32_e32 v86, 0xff0000, v86
	v_perm_b32 v84, v87, v84, s15
	v_or3_b32 v84, v84, v85, v86
	v_mul_f32_e32 v85, v81, v35
	global_store_dword v[82:83], v84, off offset:1536 sc1
	v_mul_f32_e32 v84, v81, v34
	v_mul_f32_e32 v86, v81, v36
	v_mul_f32_e32 v81, v81, v37
	v_med3_f32 v85, v85, s14, v79
	v_med3_f32 v84, v84, s14, v79
	v_rndne_f32_e32 v85, v85
	v_med3_f32 v86, v86, s14, v79
	v_med3_f32 v81, v81, s14, v79
	v_rndne_f32_e32 v84, v84
	v_cvt_i32_f32_e32 v85, v85
	v_rndne_f32_e32 v86, v86
	v_rndne_f32_e32 v81, v81
	v_cvt_i32_f32_e32 v84, v84
	v_cvt_i32_f32_sdwa v86, v86 dst_sel:WORD_1 dst_unused:UNUSED_PAD src0_sel:DWORD
	v_cvt_i32_f32_e32 v81, v81
	v_lshlrev_b32_e32 v85, 8, v85
	v_and_b32_e32 v85, 0xff00, v85
	v_and_b32_e32 v86, 0xff0000, v86
	v_perm_b32 v81, v81, v84, s15
	v_or3_b32 v81, v81, v85, v86
	global_store_dword v[82:83], v81, off offset:1792 sc1
	s_and_saveexec_b64 s[8:9], s[0:1]
	s_cbranch_execz .LBB0_17
	v_lshl_add_u64 v[82:83], s[12:13], 0, v[66:67]
	v_mul_f32_e32 v80, 0x3c010204, v80
	global_store_dword v[82:83], v80, off sc1
	s_branch .LBB0_17
.LBB0_20:
	v_lshlrev_b32_e32 v34, 4, v72
	v_lshl_or_b32 v1, v1, 13, v34
	ds_write_b128 v1, v[6:9]
	ds_write_b128 v1, v[10:13] offset:1024
	ds_write_b128 v1, v[14:17] offset:2048
	ds_write_b128 v1, v[18:21] offset:3072
	ds_write_b128 v1, v[22:25] offset:4096
	ds_write_b128 v1, v[26:29] offset:5120
	ds_write_b128 v1, v[30:33] offset:6144
	ds_write_b128 v1, v[2:5] offset:7168
	v_lshlrev_b32_e32 v32, 5, v0
	s_ashr_i32 s3, s2, 31
	s_waitcnt lgkmcnt(0)
	s_barrier
	ds_read_b128 v[0:3], v32
	ds_read_b128 v[4:7], v32 offset:16
	ds_read_b128 v[8:11], v32 offset:8192
	ds_read_b128 v[12:15], v32 offset:8208
	ds_read_b128 v[16:19], v32 offset:16384
	ds_read_b128 v[20:23], v32 offset:16400
	ds_read_b128 v[24:27], v32 offset:24576
	ds_read_b128 v[28:31], v32 offset:24592
	s_lshl_b64 s[0:1], s[2:3], 13
	s_add_u32 s0, s12, s0
	s_addc_u32 s1, s13, s1
	v_mov_b32_e32 v33, 0
	v_lshl_add_u64 v[32:33], s[0:1], 0, v[32:33]
	s_mov_b64 s[0:1], 0xd400000
	v_lshl_add_u64 v[34:35], v[32:33], 0, s[0:1]
	s_waitcnt lgkmcnt(5)
	v_pk_add_f32 v[2:3], v[2:3], v[10:11]
	v_pk_add_f32 v[0:1], v[0:1], v[8:9]
	s_waitcnt lgkmcnt(1)
	v_pk_add_f32 v[8:9], v[18:19], v[26:27]
	s_mov_b32 s0, 0xd400000
	v_pk_add_f32 v[10:11], v[16:17], v[24:25]
	v_pk_add_f32 v[2:3], v[2:3], v[8:9]
	v_add_co_u32_e32 v8, vcc, s0, v32
	v_pk_add_f32 v[0:1], v[0:1], v[10:11]
	s_nop 0
	v_addc_co_u32_e32 v9, vcc, 0, v33, vcc
	global_store_dwordx4 v[8:9], v[0:3], off sc1
	v_pk_add_f32 v[4:5], v[4:5], v[12:13]
	s_nop 0
	v_pk_add_f32 v[0:1], v[6:7], v[14:15]
	s_waitcnt lgkmcnt(0)
	v_pk_add_f32 v[2:3], v[22:23], v[30:31]
	v_pk_add_f32 v[6:7], v[20:21], v[28:29]
	v_pk_add_f32 v[2:3], v[0:1], v[2:3]
	v_pk_add_f32 v[0:1], v[4:5], v[6:7]
	global_store_dwordx4 v[34:35], v[0:3], off offset:16 sc1
	s_endpgm
	.p2align	8

.LBB1_3:
	s_cmpk_gt_u32 s2, 0x2ff
	s_cbranch_scc0 .LBB1_19
	s_cmpk_lt_u32 s2, 0x500
	s_cbranch_scc0 .LBB1_14
	s_lshl_b32 s3, s2, 4
	s_addk_i32 s3, 0xd000
	s_waitcnt lgkmcnt(0)
	s_add_u32 s4, s6, 0xd00c000
	v_lshrrev_b32_e32 v1, 4, v0
	s_addc_u32 s5, s7, 0
	v_mov_b32_e32 v35, 0
	v_and_or_b32 v62, v1, 12, s3
	s_add_u32 s8, s6, 0x4800000
	v_mov_b32_e32 v63, v35
	v_and_b32_e32 v78, 63, v0
	s_addc_u32 s9, s7, 0
	v_lshlrev_b64 v[2:3], 11, v[62:63]
	v_lshlrev_b32_e32 v34, 4, v78
	v_lshl_add_u64 v[2:3], s[8:9], 0, v[2:3]
	v_lshl_add_u64 v[2:3], v[2:3], 0, v[34:35]
	global_load_dwordx4 v[30:33], v[2:3], off
	global_load_dwordx4 v[26:29], v[2:3], off offset:1024
	v_lshlrev_b32_e32 v1, 6, v78
	global_load_dwordx4 v[10:13], v1, s[4:5]
	global_load_dwordx4 v[6:9], v1, s[4:5] offset:16
	global_load_dwordx4 v[2:5], v1, s[4:5] offset:32
	v_or_b32_e32 v56, 0x1000, v1
	global_load_dwordx4 v[14:17], v1, s[4:5] offset:48
	global_load_dwordx4 v[18:21], v56, s[4:5]
	v_mov_b32_e32 v65, v35
	v_mov_b32_e32 v61, v35
	v_mov_b32_e32 v59, v35
	v_or_b32_e32 v64, 1, v62
	v_or_b32_e32 v60, 2, v62
	v_or_b32_e32 v58, 3, v62
	v_lshlrev_b64 v[36:37], 11, v[64:65]
	v_lshlrev_b64 v[38:39], 11, v[60:61]
	v_lshlrev_b64 v[40:41], 11, v[58:59]
	v_lshl_add_u64 v[36:37], s[8:9], 0, v[36:37]
	v_lshl_add_u64 v[38:39], s[8:9], 0, v[38:39]
	v_lshl_add_u64 v[40:41], s[8:9], 0, v[40:41]
	v_lshl_add_u64 v[36:37], v[36:37], 0, v[34:35]
	v_lshl_add_u64 v[38:39], v[38:39], 0, v[34:35]
	v_lshl_add_u64 v[66:67], v[40:41], 0, v[34:35]
	global_load_dwordx4 v[22:25], v56, s[4:5] offset:16
	s_add_u32 s8, s6, 0xd010000
	s_addc_u32 s9, s7, 0
	s_waitcnt vmcnt(7)
	v_cvt_pk_f32_fp8_e32 v[34:35], v30
	v_cvt_pk_f32_fp8_sdwa v[40:41], v30 src0_sel:WORD_1
	v_cvt_pk_f32_fp8_e32 v[42:43], v31
	v_cvt_pk_f32_fp8_sdwa v[44:45], v31 src0_sel:WORD_1
	v_cvt_pk_f32_fp8_e32 v[30:31], v32
	v_cvt_pk_f32_fp8_sdwa v[46:47], v32 src0_sel:WORD_1
	v_cvt_pk_f32_fp8_e32 v[48:49], v33
	v_cvt_pk_f32_fp8_sdwa v[68:69], v33 src0_sel:WORD_1
	s_waitcnt vmcnt(6)
	v_cvt_pk_f32_fp8_e32 v[32:33], v26
	s_waitcnt vmcnt(3)
	v_mul_f32_e32 v80, v3, v31
	v_cvt_pk_f32_fp8_sdwa v[70:71], v26 src0_sel:WORD_1
	v_cvt_pk_f32_fp8_e32 v[50:51], v27
	s_waitcnt vmcnt(1)
	v_mul_f32_e32 v82, v19, v33
	v_cvt_pk_f32_fp8_sdwa v[72:73], v27 src0_sel:WORD_1
	v_cvt_pk_f32_fp8_e32 v[52:53], v28
	v_cvt_pk_f32_fp8_sdwa v[74:75], v28 src0_sel:WORD_1
	v_cvt_pk_f32_fp8_e32 v[54:55], v29
	v_cvt_pk_f32_fp8_sdwa v[76:77], v29 src0_sel:WORD_1
	v_fmac_f32_e32 v80, v2, v30
	v_fmac_f32_e32 v82, v18, v32
	global_load_dwordx4 v[30:33], v56, s[4:5] offset:32
	global_load_dwordx4 v[26:29], v56, s[4:5] offset:48
	v_mul_f32_e32 v1, v11, v35
	v_mul_f32_e32 v79, v7, v43
	v_fmac_f32_e32 v1, v10, v34
	v_fmac_f32_e32 v79, v6, v42
	v_mul_f32_e32 v81, v15, v49
	s_waitcnt vmcnt(2)
	v_mul_f32_e32 v83, v23, v51
	v_fmac_f32_e32 v1, v12, v40
	v_fmac_f32_e32 v79, v8, v44
	v_fmac_f32_e32 v80, v4, v46
	v_fmac_f32_e32 v81, v14, v48
	v_fmac_f32_e32 v83, v22, v50
	v_fmac_f32_e32 v1, v13, v41
	v_fmac_f32_e32 v79, v9, v45
	v_fmac_f32_e32 v80, v5, v47
	v_fmac_f32_e32 v82, v20, v70
	v_add_f32_e32 v1, 0, v1
	v_fmac_f32_e32 v81, v16, v68
	v_fmac_f32_e32 v81, v17, v69
	v_fmac_f32_e32 v83, v24, v72
	v_fmac_f32_e32 v82, v21, v71
	v_fmac_f32_e32 v83, v25, v73
	v_cmp_eq_u32_e64 s[4:5], 0, v78
	s_waitcnt vmcnt(1)
	v_mul_f32_e32 v84, v31, v53
	s_waitcnt vmcnt(0)
	v_mul_f32_e32 v85, v27, v55
	v_fmac_f32_e32 v84, v30, v52
	v_fmac_f32_e32 v85, v26, v54
	global_load_dwordx4 v[54:57], v[36:37], off
	global_load_dwordx4 v[50:53], v[36:37], off offset:1024
	global_load_dwordx4 v[46:49], v[38:39], off
	global_load_dwordx4 v[42:45], v[38:39], off offset:1024
	s_nop 0
	global_load_dwordx4 v[38:41], v[66:67], off
	global_load_dwordx4 v[34:37], v[66:67], off offset:1024
	v_mbcnt_lo_u32_b32 v66, -1, 0
	v_mbcnt_hi_u32_b32 v70, -1, v66
	v_and_b32_e32 v66, 64, v70
	v_add_f32_e32 v67, v1, v79
	v_add_u32_e32 v72, 64, v66
	v_add_f32_e32 v66, v67, v80
	v_add_f32_e32 v66, v66, v81
	v_fmac_f32_e32 v84, v32, v74
	v_xor_b32_e32 v1, 32, v70
	v_add_f32_e32 v66, v66, v82
	v_fmac_f32_e32 v84, v33, v75
	v_fmac_f32_e32 v85, v28, v76
	v_cmp_lt_i32_e32 vcc, v1, v72
	v_add_f32_e32 v66, v66, v83
	v_fmac_f32_e32 v85, v29, v77
	v_cndmask_b32_e32 v1, v70, v1, vcc
	v_add_f32_e32 v66, v66, v84
	v_lshlrev_b32_e32 v1, 2, v1
	v_add_f32_e32 v67, v66, v85
	ds_bpermute_b32 v68, v1, v67
	v_xor_b32_e32 v66, 16, v70
	v_cmp_lt_i32_e32 vcc, v66, v72
	v_xor_b32_e32 v74, 1, v70
	s_waitcnt lgkmcnt(0)
	v_add_f32_e32 v68, v67, v68
	v_cndmask_b32_e32 v66, v70, v66, vcc
	v_lshlrev_b32_e32 v66, 2, v66
	ds_bpermute_b32 v69, v66, v68
	v_xor_b32_e32 v67, 8, v70
	v_cmp_lt_i32_e32 vcc, v67, v72
	s_waitcnt lgkmcnt(0)
	v_add_f32_e32 v69, v68, v69
	v_cndmask_b32_e32 v67, v70, v67, vcc
	v_lshlrev_b32_e32 v67, 2, v67
	ds_bpermute_b32 v71, v67, v69
	v_xor_b32_e32 v68, 4, v70
	v_cmp_lt_i32_e32 vcc, v68, v72
	s_waitcnt lgkmcnt(0)
	v_add_f32_e32 v71, v69, v71
	v_cndmask_b32_e32 v68, v70, v68, vcc
	v_lshlrev_b32_e32 v68, 2, v68
	ds_bpermute_b32 v73, v68, v71
	v_xor_b32_e32 v69, 2, v70
	v_cmp_lt_i32_e32 vcc, v69, v72
	s_waitcnt lgkmcnt(0)
	v_add_f32_e32 v71, v71, v73
	v_cndmask_b32_e32 v69, v70, v69, vcc
	v_lshlrev_b32_e32 v69, 2, v69
	ds_bpermute_b32 v73, v69, v71
	v_cmp_lt_i32_e32 vcc, v74, v72
	s_waitcnt lgkmcnt(0)
	v_add_f32_e32 v71, v71, v73
	v_cndmask_b32_e32 v70, v70, v74, vcc
	v_lshlrev_b32_e32 v70, 2, v70
	ds_bpermute_b32 v72, v70, v71
	s_and_saveexec_b64 s[10:11], s[4:5]
	s_cbranch_execz .LBB1_7
	s_waitcnt lgkmcnt(0)
	v_add_f32_e32 v71, v71, v72
	s_mov_b32 s3, 0x47800000
	v_div_scale_f32 v72, s[12:13], v71, v71, s3
	v_rcp_f32_e32 v73, v72
	v_lshl_add_u64 v[62:63], v[62:63], 2, s[8:9]
	v_fma_f32 v74, -v72, v73, 1.0
	v_fmac_f32_e32 v73, v74, v73
	v_div_scale_f32 v74, vcc, s3, v71, s3
	v_mul_f32_e32 v75, v74, v73
	v_fma_f32 v76, -v72, v75, v74
	v_fmac_f32_e32 v75, v76, v73
	v_fma_f32 v72, -v72, v75, v74
	v_div_fmas_f32 v72, v72, v73, v75
	v_div_fixup_f32 v71, v72, v71, s3
	global_store_dword v[62:63], v71, off sc1
.LBB1_7:
	s_or_b64 exec, exec, s[10:11]
	s_waitcnt vmcnt(5)
	v_cvt_pk_f32_fp8_e32 v[62:63], v54
	s_waitcnt lgkmcnt(0)
	v_cvt_pk_f32_fp8_sdwa v[72:73], v54 src0_sel:WORD_1
	v_cvt_pk_f32_fp8_e32 v[74:75], v55
	v_cvt_pk_f32_fp8_sdwa v[54:55], v55 src0_sel:WORD_1
	v_mul_f32_e32 v63, v11, v63
	v_fmac_f32_e32 v63, v10, v62
	v_fmac_f32_e32 v63, v12, v72
	v_fmac_f32_e32 v63, v13, v73
	v_mul_f32_e32 v72, v7, v75
	v_add_f32_e32 v71, 0, v63
	v_fmac_f32_e32 v72, v6, v74
	v_cvt_pk_f32_fp8_e32 v[62:63], v56
	v_fmac_f32_e32 v72, v8, v54
	v_fmac_f32_e32 v72, v9, v55
	v_cvt_pk_f32_fp8_sdwa v[54:55], v56 src0_sel:WORD_1
	v_add_f32_e32 v56, v71, v72
	v_mul_f32_e32 v71, v3, v63
	v_fmac_f32_e32 v71, v2, v62
	v_cvt_pk_f32_fp8_e32 v[62:63], v57
	v_fmac_f32_e32 v71, v4, v54
	v_fmac_f32_e32 v71, v5, v55
	v_cvt_pk_f32_fp8_sdwa v[54:55], v57 src0_sel:WORD_1
	v_add_f32_e32 v71, v56, v71
	v_mul_f32_e32 v63, v15, v63
	s_waitcnt vmcnt(4)
	v_cvt_pk_f32_fp8_e32 v[56:57], v50
	v_fmac_f32_e32 v63, v14, v62
	v_fmac_f32_e32 v63, v16, v54
	v_fmac_f32_e32 v63, v17, v55
	v_add_f32_e32 v62, v71, v63
	v_mul_f32_e32 v63, v19, v57
	v_cvt_pk_f32_fp8_sdwa v[54:55], v50 src0_sel:WORD_1
	v_fmac_f32_e32 v63, v18, v56
	v_cvt_pk_f32_fp8_e32 v[56:57], v51
	v_cvt_pk_f32_fp8_sdwa v[50:51], v51 src0_sel:WORD_1
	v_fmac_f32_e32 v63, v20, v54
	v_fmac_f32_e32 v63, v21, v55
	v_mul_f32_e32 v57, v23, v57
	v_fmac_f32_e32 v57, v22, v56
	v_cvt_pk_f32_fp8_e32 v[54:55], v52
	v_fmac_f32_e32 v57, v24, v50
	v_fmac_f32_e32 v57, v25, v51
	v_cvt_pk_f32_fp8_sdwa v[50:51], v52 src0_sel:WORD_1
	v_mul_f32_e32 v56, v31, v55
	v_fmac_f32_e32 v56, v30, v54
	v_cvt_pk_f32_fp8_e32 v[54:55], v53
	v_fmac_f32_e32 v56, v32, v50
	v_fmac_f32_e32 v56, v33, v51
	v_cvt_pk_f32_fp8_sdwa v[50:51], v53 src0_sel:WORD_1
	v_mul_f32_e32 v53, v27, v55
	v_add_f32_e32 v62, v62, v63
	v_fmac_f32_e32 v53, v26, v54
	v_add_f32_e32 v52, v62, v57
	v_fmac_f32_e32 v53, v28, v50
	v_add_f32_e32 v52, v52, v56
	v_fmac_f32_e32 v53, v29, v51
	v_add_f32_e32 v50, v52, v53
	ds_bpermute_b32 v51, v1, v50
	s_waitcnt lgkmcnt(0)
	v_add_f32_e32 v50, v50, v51
	ds_bpermute_b32 v51, v66, v50
	s_waitcnt lgkmcnt(0)
	v_add_f32_e32 v50, v50, v51
	ds_bpermute_b32 v51, v67, v50
	s_waitcnt lgkmcnt(0)
	v_add_f32_e32 v50, v50, v51
	ds_bpermute_b32 v51, v68, v50
	s_waitcnt lgkmcnt(0)
	v_add_f32_e32 v50, v50, v51
	ds_bpermute_b32 v51, v69, v50
	s_waitcnt lgkmcnt(0)
	v_add_f32_e32 v50, v50, v51
	ds_bpermute_b32 v51, v70, v50
	s_and_saveexec_b64 s[10:11], s[4:5]
	s_cbranch_execz .LBB1_9
	s_waitcnt lgkmcnt(0)
	v_add_f32_e32 v50, v50, v51
	s_mov_b32 s3, 0x47800000
	v_div_scale_f32 v51, s[12:13], v50, v50, s3
	v_rcp_f32_e32 v52, v51
	s_nop 0
	v_fma_f32 v53, -v51, v52, 1.0
	v_fmac_f32_e32 v52, v53, v52
	v_div_scale_f32 v53, vcc, s3, v50, s3
	v_mul_f32_e32 v54, v53, v52
	v_fma_f32 v55, -v51, v54, v53
	v_fmac_f32_e32 v54, v55, v52
	v_fma_f32 v51, -v51, v54, v53
	v_div_fmas_f32 v51, v51, v52, v54
	v_div_fixup_f32 v52, v51, v50, s3
	v_lshl_add_u64 v[50:51], v[64:65], 2, s[8:9]
	global_store_dword v[50:51], v52, off sc1
.LBB1_9:
	s_or_b64 exec, exec, s[10:11]
	s_waitcnt vmcnt(3) lgkmcnt(0)
	v_cvt_pk_f32_fp8_e32 v[50:51], v46
	v_cvt_pk_f32_fp8_sdwa v[52:53], v46 src0_sel:WORD_1
	v_cvt_pk_f32_fp8_e32 v[54:55], v47
	v_cvt_pk_f32_fp8_sdwa v[46:47], v47 src0_sel:WORD_1
	v_mul_f32_e32 v51, v11, v51
	v_fmac_f32_e32 v51, v10, v50
	v_fmac_f32_e32 v51, v12, v52
	v_fmac_f32_e32 v51, v13, v53
	v_mul_f32_e32 v53, v7, v55
	v_add_f32_e32 v52, 0, v51
	v_fmac_f32_e32 v53, v6, v54
	v_cvt_pk_f32_fp8_e32 v[50:51], v48
	v_fmac_f32_e32 v53, v8, v46
	v_fmac_f32_e32 v53, v9, v47
	v_cvt_pk_f32_fp8_sdwa v[46:47], v48 src0_sel:WORD_1
	v_add_f32_e32 v48, v52, v53
	v_mul_f32_e32 v52, v3, v51
	v_fmac_f32_e32 v52, v2, v50
	v_cvt_pk_f32_fp8_e32 v[50:51], v49
	v_fmac_f32_e32 v52, v4, v46
	v_fmac_f32_e32 v52, v5, v47
	v_cvt_pk_f32_fp8_sdwa v[46:47], v49 src0_sel:WORD_1
	v_add_f32_e32 v52, v48, v52
	v_mul_f32_e32 v51, v15, v51
	s_waitcnt vmcnt(2)
	v_cvt_pk_f32_fp8_e32 v[48:49], v42
	v_fmac_f32_e32 v51, v14, v50
	v_fmac_f32_e32 v51, v16, v46
	v_fmac_f32_e32 v51, v17, v47
	v_add_f32_e32 v50, v52, v51
	v_mul_f32_e32 v51, v19, v49
	v_cvt_pk_f32_fp8_sdwa v[46:47], v42 src0_sel:WORD_1
	v_fmac_f32_e32 v51, v18, v48
	v_cvt_pk_f32_fp8_e32 v[48:49], v43
	v_cvt_pk_f32_fp8_sdwa v[42:43], v43 src0_sel:WORD_1
	v_fmac_f32_e32 v51, v20, v46
	v_fmac_f32_e32 v51, v21, v47
	v_mul_f32_e32 v49, v23, v49
	v_fmac_f32_e32 v49, v22, v48
	v_cvt_pk_f32_fp8_e32 v[46:47], v44
	v_fmac_f32_e32 v49, v24, v42
	v_fmac_f32_e32 v49, v25, v43
	v_cvt_pk_f32_fp8_sdwa v[42:43], v44 src0_sel:WORD_1
	v_mul_f32_e32 v48, v31, v47
	v_fmac_f32_e32 v48, v30, v46
	v_cvt_pk_f32_fp8_e32 v[46:47], v45
	v_fmac_f32_e32 v48, v32, v42
	v_fmac_f32_e32 v48, v33, v43
	v_cvt_pk_f32_fp8_sdwa v[42:43], v45 src0_sel:WORD_1
	v_mul_f32_e32 v45, v27, v47
	v_add_f32_e32 v50, v50, v51
	v_fmac_f32_e32 v45, v26, v46
	v_add_f32_e32 v44, v50, v49
	v_fmac_f32_e32 v45, v28, v42
	v_add_f32_e32 v44, v44, v48
	v_fmac_f32_e32 v45, v29, v43
	v_add_f32_e32 v42, v44, v45
	ds_bpermute_b32 v43, v1, v42
	s_waitcnt lgkmcnt(0)
	v_add_f32_e32 v42, v42, v43
	ds_bpermute_b32 v43, v66, v42
	s_waitcnt lgkmcnt(0)
	v_add_f32_e32 v42, v42, v43
	ds_bpermute_b32 v43, v67, v42
	s_waitcnt lgkmcnt(0)
	v_add_f32_e32 v42, v42, v43
	ds_bpermute_b32 v43, v68, v42
	s_waitcnt lgkmcnt(0)
	v_add_f32_e32 v42, v42, v43
	ds_bpermute_b32 v43, v69, v42
	s_waitcnt lgkmcnt(0)
	v_add_f32_e32 v42, v42, v43
	ds_bpermute_b32 v43, v70, v42
	s_and_saveexec_b64 s[10:11], s[4:5]
	s_cbranch_execz .LBB1_11
	s_waitcnt lgkmcnt(0)
	v_add_f32_e32 v42, v42, v43
	s_mov_b32 s3, 0x47800000
	v_div_scale_f32 v43, s[12:13], v42, v42, s3
	v_rcp_f32_e32 v44, v43
	s_nop 0
	v_fma_f32 v45, -v43, v44, 1.0
	v_fmac_f32_e32 v44, v45, v44
	v_div_scale_f32 v45, vcc, s3, v42, s3
	v_mul_f32_e32 v46, v45, v44
	v_fma_f32 v47, -v43, v46, v45
	v_fmac_f32_e32 v46, v47, v44
	v_fma_f32 v43, -v43, v46, v45
	v_div_fmas_f32 v43, v43, v44, v46
	v_div_fixup_f32 v44, v43, v42, s3
	v_lshl_add_u64 v[42:43], v[60:61], 2, s[8:9]
	global_store_dword v[42:43], v44, off sc1
.LBB1_11:
	s_or_b64 exec, exec, s[10:11]
	s_waitcnt vmcnt(1) lgkmcnt(0)
	v_cvt_pk_f32_fp8_e32 v[42:43], v38
	v_cvt_pk_f32_fp8_sdwa v[44:45], v38 src0_sel:WORD_1
	v_cvt_pk_f32_fp8_e32 v[46:47], v39
	v_cvt_pk_f32_fp8_sdwa v[38:39], v39 src0_sel:WORD_1
	v_mul_f32_e32 v11, v11, v43
	v_fmac_f32_e32 v11, v10, v42
	v_fmac_f32_e32 v11, v12, v44
	v_fmac_f32_e32 v11, v13, v45
	v_add_f32_e32 v10, 0, v11
	v_mul_f32_e32 v11, v7, v47
	v_fmac_f32_e32 v11, v6, v46
	v_cvt_pk_f32_fp8_e32 v[6:7], v40
	v_fmac_f32_e32 v11, v8, v38
	v_fmac_f32_e32 v11, v9, v39
	v_cvt_pk_f32_fp8_sdwa v[8:9], v40 src0_sel:WORD_1
	v_mul_f32_e32 v7, v3, v7
	v_fmac_f32_e32 v7, v2, v6
	v_cvt_pk_f32_fp8_e32 v[2:3], v41
	v_fmac_f32_e32 v7, v4, v8
	v_fmac_f32_e32 v7, v5, v9
	v_cvt_pk_f32_fp8_sdwa v[4:5], v41 src0_sel:WORD_1
	v_add_f32_e32 v10, v10, v11
	v_add_f32_e32 v6, v10, v7
	v_mul_f32_e32 v7, v15, v3
	v_fmac_f32_e32 v7, v14, v2
	s_waitcnt vmcnt(0)
	v_cvt_pk_f32_fp8_e32 v[2:3], v34
	v_fmac_f32_e32 v7, v16, v4
	v_fmac_f32_e32 v7, v17, v5
	v_cvt_pk_f32_fp8_sdwa v[4:5], v34 src0_sel:WORD_1
	v_add_f32_e32 v6, v6, v7
	v_mul_f32_e32 v7, v19, v3
	v_fmac_f32_e32 v7, v18, v2
	v_cvt_pk_f32_fp8_e32 v[2:3], v35
	v_fmac_f32_e32 v7, v20, v4
	v_fmac_f32_e32 v7, v21, v5
	v_cvt_pk_f32_fp8_sdwa v[4:5], v35 src0_sel:WORD_1
	v_add_f32_e32 v6, v6, v7
	v_mul_f32_e32 v7, v23, v3
	v_fmac_f32_e32 v7, v22, v2
	v_cvt_pk_f32_fp8_e32 v[2:3], v36
	v_fmac_f32_e32 v7, v24, v4
	v_fmac_f32_e32 v7, v25, v5
	v_cvt_pk_f32_fp8_sdwa v[4:5], v36 src0_sel:WORD_1
	v_add_f32_e32 v6, v6, v7
	v_mul_f32_e32 v7, v31, v3
	v_fmac_f32_e32 v7, v30, v2
	v_cvt_pk_f32_fp8_e32 v[2:3], v37
	v_fmac_f32_e32 v7, v32, v4
	v_fmac_f32_e32 v7, v33, v5
	v_cvt_pk_f32_fp8_sdwa v[4:5], v37 src0_sel:WORD_1
	v_mul_f32_e32 v3, v27, v3
	v_fmac_f32_e32 v3, v26, v2
	v_add_f32_e32 v6, v6, v7
	v_fmac_f32_e32 v3, v28, v4
	v_fmac_f32_e32 v3, v29, v5
	v_add_f32_e32 v2, v6, v3
	ds_bpermute_b32 v1, v1, v2
	s_waitcnt lgkmcnt(0)
	v_add_f32_e32 v1, v2, v1
	ds_bpermute_b32 v2, v66, v1
	s_waitcnt lgkmcnt(0)
	v_add_f32_e32 v1, v1, v2
	ds_bpermute_b32 v2, v67, v1
	s_waitcnt lgkmcnt(0)
	v_add_f32_e32 v1, v1, v2
	ds_bpermute_b32 v2, v68, v1
	s_waitcnt lgkmcnt(0)
	v_add_f32_e32 v1, v1, v2
	ds_bpermute_b32 v2, v69, v1
	s_waitcnt lgkmcnt(0)
	v_add_f32_e32 v1, v1, v2
	ds_bpermute_b32 v2, v70, v1
	s_and_saveexec_b64 s[10:11], s[4:5]
	s_cbranch_execz .LBB1_13
	s_waitcnt lgkmcnt(0)
	v_add_f32_e32 v1, v1, v2
	s_mov_b32 s3, 0x47800000
	v_div_scale_f32 v2, s[4:5], v1, v1, s3
	v_rcp_f32_e32 v3, v2
	s_nop 0
	v_fma_f32 v4, -v2, v3, 1.0
	v_fmac_f32_e32 v3, v4, v3
	v_div_scale_f32 v4, vcc, s3, v1, s3
	v_mul_f32_e32 v5, v4, v3
	v_fma_f32 v6, -v2, v5, v4
	v_fmac_f32_e32 v5, v6, v3
	v_fma_f32 v2, -v2, v5, v4
	v_div_fmas_f32 v2, v2, v3, v5
	v_div_fixup_f32 v1, v2, v1, s3
	v_lshl_add_u64 v[2:3], v[58:59], 2, s[8:9]
	global_store_dword v[2:3], v1, off sc1

.LBB1_16:
	v_lshl_add_u64 v[6:7], v[4:5], 0, s[4:5]
	v_add_co_u32_e32 v8, vcc, 0xd01c000, v6
	s_add_u32 s4, s4, 0x10000
	s_nop 0
	v_addc_co_u32_e32 v9, vcc, 0, v7, vcc
	v_add_co_u32_e32 v10, vcc, 0xd01e000, v6
	s_addc_u32 s5, s5, 0
	s_nop 0
	v_addc_co_u32_e32 v11, vcc, 0, v7, vcc
	v_add_co_u32_e32 v12, vcc, 0xd020000, v6
	global_load_dword v1, v[8:9], off
	global_load_dword v14, v[10:11], off
	v_addc_co_u32_e32 v13, vcc, 0, v7, vcc
	v_add_co_u32_e32 v8, vcc, 0xd022000, v6
	s_cmp_eq_u32 s4, 0x40000
	s_nop 0
	v_addc_co_u32_e32 v9, vcc, 0, v7, vcc
	v_add_co_u32_e32 v10, vcc, 0xd024000, v6
	global_load_dword v15, v[12:13], off
	global_load_dword v16, v[8:9], off
	v_addc_co_u32_e32 v11, vcc, 0, v7, vcc
	v_add_co_u32_e32 v8, vcc, 0xd026000, v6
	s_waitcnt vmcnt(3)
	v_add_f32_e32 v1, v3, v1
	v_addc_co_u32_e32 v9, vcc, 0, v7, vcc
	v_add_co_u32_e32 v12, vcc, 0xd028000, v6
	global_load_dword v17, v[10:11], off
	global_load_dword v18, v[8:9], off
	v_addc_co_u32_e32 v13, vcc, 0, v7, vcc
	v_add_co_u32_e32 v6, vcc, 0xd02a000, v6
	s_waitcnt vmcnt(4)
	v_add_f32_e32 v1, v1, v14
	v_addc_co_u32_e32 v7, vcc, 0, v7, vcc
	global_load_dword v8, v[12:13], off
	global_load_dword v9, v[6:7], off
	s_waitcnt vmcnt(5)
	v_add_f32_e32 v1, v1, v15
	s_waitcnt vmcnt(4)
	v_add_f32_e32 v1, v1, v16
	s_waitcnt vmcnt(3)
	v_add_f32_e32 v1, v1, v17
	s_waitcnt vmcnt(2)
	v_add_f32_e32 v1, v1, v18
	s_waitcnt vmcnt(1)
	v_add_f32_e32 v1, v1, v8
	s_waitcnt vmcnt(0)
	v_add_f32_e32 v3, v1, v9
	s_cbranch_scc0 .LBB1_16
	v_ashrrev_i32_e32 v5, 31, v2
	v_mov_b32_e32 v4, v2
	v_lshl_add_u64 v[4:5], v[4:5], 2, s[6:7]
	v_add_co_u32_e32 v4, vcc, 0xd018000, v4
	s_nop 1
	v_addc_co_u32_e32 v5, vcc, 0, v5, vcc
	global_store_dword v[4:5], v3, off sc1

.LBB1_19:
	s_andn2_b64 vcc, exec, s[4:5]
	s_cbranch_vccnz .LBB1_21
	s_add_i32 s8, s2, 0xffffff00
	v_lshlrev_b32_e32 v38, 4, v0
	s_mov_b32 s9, 0
	v_mov_b32_e32 v39, 0
	s_waitcnt lgkmcnt(0)
	v_lshl_add_u64 v[2:3], s[6:7], 0, v[38:39]
	s_lshl_b64 s[10:11], s[8:9], 12
	v_lshl_add_u64 v[4:5], v[2:3], 0, s[10:11]
	v_add_co_u32_e32 v6, vcc, 0x400000, v4
	s_lshl_b32 s3, s2, 12
	s_nop 0
	v_addc_co_u32_e32 v7, vcc, 0, v5, vcc
	global_load_dwordx4 v[18:21], v[4:5], off nt
	global_load_dwordx4 v[22:25], v[6:7], off nt
	v_add_co_u32_e32 v6, vcc, 0x800000, v4
	s_add_i32 s8, s3, 0x100000
	s_nop 0
	v_addc_co_u32_e32 v7, vcc, 0, v5, vcc
	v_add_co_u32_e32 v4, vcc, 0xc00000, v4
	v_or_b32_e32 v40, s10, v38
	s_nop 0
	v_addc_co_u32_e32 v5, vcc, 0, v5, vcc
	v_mov_b32_e32 v41, s11
	global_load_dwordx4 v[26:29], v[6:7], off nt
	global_load_dwordx4 v[30:33], v[4:5], off nt
	s_add_u32 s4, s6, 0xd00c000
	v_lshrrev_b64 v[4:5], 9, v[40:41]
	s_addc_u32 s5, s7, 0
	v_and_b32_e32 v4, -4, v4
	v_lshl_add_u64 v[4:5], s[4:5], 0, v[4:5]
	s_movk_i32 s12, 0x2000
	v_add_co_u32_e32 v4, vcc, s12, v4
	v_lshlrev_b32_e32 v1, 6, v0
	s_nop 0
	v_addc_co_u32_e32 v5, vcc, 0, v5, vcc
	v_and_b32_e32 v1, 0x1fc0, v1
	global_load_dword v74, v[4:5], off
	global_load_dwordx4 v[42:45], v1, s[4:5]
	s_mov_b32 s3, 0x400000
	v_lshl_add_u64 v[6:7], v[2:3], 0, s[8:9]
	v_add_co_u32_e32 v8, vcc, s3, v6
	s_mov_b32 s10, 0x800000
	s_nop 0
	v_addc_co_u32_e32 v9, vcc, 0, v7, vcc
	v_add_co_u32_e32 v34, vcc, s10, v6
	s_mov_b32 s11, 0xc00000
	s_nop 0
	v_addc_co_u32_e32 v35, vcc, 0, v7, vcc
	v_add_co_u32_e32 v36, vcc, s11, v6
	global_load_dwordx4 v[10:13], v[6:7], off nt
	global_load_dwordx4 v[2:5], v[8:9], off nt
	v_addc_co_u32_e32 v37, vcc, 0, v7, vcc
	global_load_dwordx4 v[14:17], v[34:35], off nt
	global_load_dwordx4 v[6:9], v[36:37], off nt
	global_load_dwordx4 v[46:49], v1, s[4:5] offset:16
	global_load_dwordx4 v[50:53], v1, s[4:5] offset:32
	global_load_dwordx4 v[54:57], v1, s[4:5] offset:48
	s_mov_b32 s3, 0xc3e00000
	v_mov_b32_e32 v75, 0x43e00000
	s_add_u32 s10, s6, 0xa800000
	s_addc_u32 s11, s7, 0
	s_waitcnt vmcnt(12)
	v_cvt_pk_f32_fp8_e32 v[58:59], v18
	s_waitcnt vmcnt(11)
	v_cvt_pk_f32_fp8_e32 v[64:65], v22
	v_cvt_pk_f32_fp8_sdwa v[60:61], v18 src0_sel:WORD_1
	v_cvt_pk_f32_fp8_sdwa v[66:67], v22 src0_sel:WORD_1
	v_pk_add_f32 v[58:59], v[58:59], 0 op_sel_hi:[1,0]
	v_cvt_pk_f32_fp8_e32 v[62:63], v19
	v_pk_add_f32 v[58:59], v[58:59], v[64:65]
	v_pk_add_f32 v[60:61], v[60:61], 0 op_sel_hi:[1,0]
	s_waitcnt vmcnt(10)
	v_cvt_pk_f32_fp8_e32 v[70:71], v26
	v_cvt_pk_f32_fp8_sdwa v[68:69], v26 src0_sel:WORD_1
	s_waitcnt vmcnt(9)
	v_cvt_pk_f32_fp8_e32 v[72:73], v30
	v_cvt_pk_f32_fp8_sdwa v[64:65], v30 src0_sel:WORD_1
	v_pk_add_f32 v[60:61], v[60:61], v[66:67]
	v_pk_add_f32 v[58:59], v[58:59], v[70:71]
	v_pk_add_f32 v[60:61], v[60:61], v[68:69]
	v_pk_add_f32 v[58:59], v[58:59], v[72:73]
	v_pk_add_f32 v[60:61], v[60:61], v[64:65]
	s_waitcnt vmcnt(8)
	v_mul_f32_e32 v18, 0xb7000000, v74
	s_waitcnt vmcnt(7)
	v_pk_fma_f32 v[42:43], v[18:19], v[42:43], v[58:59] op_sel_hi:[0,1,1]
	v_pk_fma_f32 v[44:45], v[18:19], v[44:45], v[60:61] op_sel_hi:[0,1,1]
	v_cvt_pk_f32_fp8_sdwa v[58:59], v19 src0_sel:WORD_1
	v_med3_f32 v19, v42, s3, v75
	v_med3_f32 v22, v43, s3, v75
	v_cvt_pk_fp8_f32 v34, v19, v22
	v_cvt_pk_f32_fp8_e32 v[42:43], v23
	v_cvt_pk_f32_fp8_sdwa v[22:23], v23 src0_sel:WORD_1
	v_pk_add_f32 v[58:59], v[58:59], 0 op_sel_hi:[1,0]
	v_pk_add_f32 v[60:61], v[62:63], 0 op_sel_hi:[1,0]
	v_pk_add_f32 v[22:23], v[58:59], v[22:23]
	v_cvt_pk_f32_fp8_sdwa v[58:59], v27 src0_sel:WORD_1
	v_cvt_pk_f32_fp8_e32 v[26:27], v27
	v_pk_add_f32 v[42:43], v[60:61], v[42:43]
	v_cvt_pk_f32_fp8_e32 v[60:61], v31
	v_cvt_pk_f32_fp8_sdwa v[30:31], v31 src0_sel:WORD_1
	v_pk_add_f32 v[22:23], v[22:23], v[58:59]
	v_pk_add_f32 v[26:27], v[42:43], v[26:27]
	v_cvt_pk_f32_fp8_sdwa v[42:43], v24 src0_sel:WORD_1
	v_pk_add_f32 v[26:27], v[26:27], v[60:61]
	v_pk_add_f32 v[22:23], v[22:23], v[30:31]
	s_waitcnt vmcnt(2)
	v_pk_fma_f32 v[26:27], v[18:19], v[46:47], v[26:27] op_sel_hi:[0,1,1]
	v_pk_fma_f32 v[22:23], v[18:19], v[48:49], v[22:23] op_sel_hi:[0,1,1]
	v_med3_f32 v19, v44, s3, v75
	v_med3_f32 v30, v45, s3, v75
	v_cvt_pk_fp8_f32 v34, v19, v30 op_sel:[0,0,1]
	v_med3_f32 v19, v26, s3, v75
	v_med3_f32 v26, v27, s3, v75
	v_cvt_pk_fp8_f32 v35, v19, v26
	v_med3_f32 v19, v22, s3, v75
	v_med3_f32 v30, v23, s3, v75
	v_cvt_pk_f32_fp8_e32 v[22:23], v20
	v_cvt_pk_f32_fp8_e32 v[26:27], v24
	v_cvt_pk_fp8_f32 v35, v19, v30 op_sel:[0,0,1]
	v_cvt_pk_f32_fp8_sdwa v[30:31], v20 src0_sel:WORD_1
	v_pk_add_f32 v[22:23], v[22:23], 0 op_sel_hi:[1,0]
	v_cvt_pk_f32_fp8_e32 v[44:45], v32
	v_pk_add_f32 v[22:23], v[22:23], v[26:27]
	v_pk_add_f32 v[26:27], v[30:31], 0 op_sel_hi:[1,0]
	v_cvt_pk_f32_fp8_sdwa v[30:31], v28 src0_sel:WORD_1
	v_pk_add_f32 v[26:27], v[26:27], v[42:43]
	v_cvt_pk_f32_fp8_e32 v[42:43], v28
	v_cvt_pk_f32_fp8_sdwa v[46:47], v32 src0_sel:WORD_1
	v_pk_add_f32 v[26:27], v[26:27], v[30:31]
	v_cvt_pk_f32_fp8_sdwa v[30:31], v33 src0_sel:WORD_1
	v_pk_add_f32 v[22:23], v[22:23], v[42:43]
	v_pk_add_f32 v[26:27], v[26:27], v[46:47]
	v_pk_add_f32 v[22:23], v[22:23], v[44:45]
	v_cvt_pk_f32_fp8_e32 v[42:43], v14
	s_waitcnt vmcnt(1)
	v_pk_fma_f32 v[22:23], v[18:19], v[50:51], v[22:23] op_sel_hi:[0,1,1]
	v_med3_f32 v19, v22, s3, v75
	v_med3_f32 v20, v23, s3, v75
	v_cvt_pk_fp8_f32 v36, v19, v20
	v_pk_fma_f32 v[22:23], v[18:19], v[52:53], v[26:27] op_sel_hi:[0,1,1]
	v_med3_f32 v19, v22, s3, v75
	v_med3_f32 v20, v23, s3, v75
	v_cvt_pk_fp8_f32 v36, v19, v20 op_sel:[0,0,1]
	v_cvt_pk_f32_fp8_sdwa v[22:23], v21 src0_sel:WORD_1
	v_cvt_pk_f32_fp8_e32 v[20:21], v21
	v_cvt_pk_f32_fp8_e32 v[26:27], v25
	v_cvt_pk_f32_fp8_sdwa v[24:25], v25 src0_sel:WORD_1
	v_pk_add_f32 v[22:23], v[22:23], 0 op_sel_hi:[1,0]
	v_pk_add_f32 v[20:21], v[20:21], 0 op_sel_hi:[1,0]
	v_or_b32_e32 v50, s8, v38
	v_pk_add_f32 v[20:21], v[20:21], v[26:27]
	v_cvt_pk_f32_fp8_e32 v[26:27], v29
	v_pk_add_f32 v[22:23], v[22:23], v[24:25]
	v_cvt_pk_f32_fp8_sdwa v[24:25], v29 src0_sel:WORD_1
	v_cvt_pk_f32_fp8_e32 v[28:29], v33
	v_pk_add_f32 v[20:21], v[20:21], v[26:27]
	v_cvt_pk_f32_fp8_sdwa v[44:45], v14 src0_sel:WORD_1
	v_pk_add_f32 v[22:23], v[22:23], v[24:25]
	v_pk_add_f32 v[20:21], v[20:21], v[28:29]
	v_pk_add_f32 v[22:23], v[22:23], v[30:31]
	s_waitcnt vmcnt(0)
	v_pk_fma_f32 v[20:21], v[18:19], v[54:55], v[20:21] op_sel_hi:[0,1,1]
	v_med3_f32 v19, v20, s3, v75
	v_med3_f32 v20, v21, s3, v75
	v_cvt_pk_fp8_f32 v37, v19, v20
	v_pk_fma_f32 v[18:19], v[18:19], v[56:57], v[22:23] op_sel_hi:[0,1,1]
	v_med3_f32 v18, v18, s3, v75
	v_med3_f32 v19, v19, s3, v75
	v_cvt_pk_fp8_f32 v37, v18, v19 op_sel:[0,0,1]
	v_lshl_add_u64 v[18:19], s[10:11], 0, v[40:41]
	v_cvt_pk_f32_fp8_sdwa v[24:25], v10 src0_sel:WORD_1
	v_cvt_pk_f32_fp8_e32 v[46:47], v6
	global_store_dwordx4 v[18:19], v[34:37], off sc1
	v_lshrrev_b32_e32 v18, 9, v50
	v_and_b32_e32 v38, 0x3ffffc, v18
	v_lshl_add_u64 v[18:19], s[4:5], 0, v[38:39]
	v_add_co_u32_e32 v22, vcc, s12, v18
	v_cvt_pk_f32_fp8_e32 v[34:35], v10
	s_nop 0
	v_addc_co_u32_e32 v23, vcc, 0, v19, vcc
	global_load_dword v51, v[22:23], off
	global_load_dwordx4 v[18:21], v1, s[4:5]
	global_load_dwordx4 v[26:29], v1, s[4:5] offset:16
	global_load_dwordx4 v[30:33], v1, s[4:5] offset:32
	v_cvt_pk_f32_fp8_e32 v[36:37], v2
	v_cvt_pk_f32_fp8_sdwa v[38:39], v2 src0_sel:WORD_1
	v_pk_add_f32 v[24:25], v[24:25], 0 op_sel_hi:[1,0]
	v_pk_add_f32 v[34:35], v[34:35], 0 op_sel_hi:[1,0]
	v_cvt_pk_f32_fp8_sdwa v[48:49], v6 src0_sel:WORD_1
	v_pk_add_f32 v[40:41], v[34:35], v[36:37]
	v_pk_add_f32 v[38:39], v[24:25], v[38:39]
	global_load_dwordx4 v[34:37], v1, s[4:5] offset:48
	v_pk_add_f32 v[40:41], v[40:41], v[42:43]
	v_pk_add_f32 v[38:39], v[38:39], v[44:45]
	v_pk_add_f32 v[40:41], v[40:41], v[46:47]
	v_pk_add_f32 v[38:39], v[38:39], v[48:49]
	s_waitcnt vmcnt(4)
	v_mul_f32_e32 v2, 0xb7000000, v51
	s_waitcnt vmcnt(3)
	v_pk_fma_f32 v[18:19], v[2:3], v[18:19], v[40:41] op_sel_hi:[0,1,1]
	v_med3_f32 v1, v18, s3, v75
	v_med3_f32 v6, v19, s3, v75
	v_pk_fma_f32 v[18:19], v[2:3], v[20:21], v[38:39] op_sel_hi:[0,1,1]
	v_cvt_pk_fp8_f32 v22, v1, v6
	v_med3_f32 v1, v18, s3, v75
	v_med3_f32 v6, v19, s3, v75
	v_cvt_pk_f32_fp8_sdwa v[18:19], v11 src0_sel:WORD_1
	v_cvt_pk_f32_fp8_e32 v[10:11], v11
	v_cvt_pk_f32_fp8_e32 v[20:21], v3
	v_cvt_pk_f32_fp8_sdwa v[38:39], v3 src0_sel:WORD_1
	v_pk_add_f32 v[18:19], v[18:19], 0 op_sel_hi:[1,0]
	v_pk_add_f32 v[10:11], v[10:11], 0 op_sel_hi:[1,0]
	v_cvt_pk_fp8_f32 v22, v1, v6 op_sel:[0,0,1]
	v_pk_add_f32 v[10:11], v[10:11], v[20:21]
	v_cvt_pk_f32_fp8_sdwa v[20:21], v15 src0_sel:WORD_1
	v_cvt_pk_f32_fp8_e32 v[14:15], v15
	v_pk_add_f32 v[18:19], v[18:19], v[38:39]
	v_cvt_pk_f32_fp8_e32 v[38:39], v7
	v_cvt_pk_f32_fp8_sdwa v[6:7], v7 src0_sel:WORD_1
	v_pk_add_f32 v[10:11], v[10:11], v[14:15]
	v_pk_add_f32 v[18:19], v[18:19], v[20:21]
	v_pk_add_f32 v[10:11], v[10:11], v[38:39]
	v_pk_add_f32 v[6:7], v[18:19], v[6:7]
	s_waitcnt vmcnt(2)
	v_pk_fma_f32 v[10:11], v[2:3], v[26:27], v[10:11] op_sel_hi:[0,1,1]
	v_med3_f32 v3, v11, s3, v75
	v_med3_f32 v1, v10, s3, v75
	v_pk_fma_f32 v[6:7], v[2:3], v[28:29], v[6:7] op_sel_hi:[0,1,1]
	v_cvt_pk_fp8_f32 v23, v1, v3
	v_med3_f32 v1, v6, s3, v75
	v_med3_f32 v3, v7, s3, v75
	v_cvt_pk_f32_fp8_sdwa v[6:7], v12 src0_sel:WORD_1
	v_cvt_pk_f32_fp8_sdwa v[18:19], v4 src0_sel:WORD_1
	v_cvt_pk_f32_fp8_e32 v[10:11], v12
	v_cvt_pk_f32_fp8_e32 v[14:15], v4
	v_pk_add_f32 v[6:7], v[6:7], 0 op_sel_hi:[1,0]
	v_cvt_pk_f32_fp8_e32 v[20:21], v8
	v_pk_add_f32 v[6:7], v[6:7], v[18:19]
	v_cvt_pk_f32_fp8_e32 v[18:19], v16
	v_pk_add_f32 v[10:11], v[10:11], 0 op_sel_hi:[1,0]
	v_cvt_pk_f32_fp8_sdwa v[26:27], v8 src0_sel:WORD_1
	v_pk_add_f32 v[10:11], v[10:11], v[14:15]
	v_cvt_pk_f32_fp8_sdwa v[14:15], v16 src0_sel:WORD_1
	v_pk_add_f32 v[10:11], v[10:11], v[18:19]
	v_cvt_pk_fp8_f32 v23, v1, v3 op_sel:[0,0,1]
	v_pk_add_f32 v[10:11], v[10:11], v[20:21]
	v_pk_add_f32 v[6:7], v[6:7], v[14:15]
	s_waitcnt vmcnt(1)
	v_pk_fma_f32 v[10:11], v[2:3], v[30:31], v[10:11] op_sel_hi:[0,1,1]
	v_pk_add_f32 v[6:7], v[6:7], v[26:27]
	v_med3_f32 v3, v11, s3, v75
	v_med3_f32 v1, v10, s3, v75
	v_pk_fma_f32 v[6:7], v[2:3], v[32:33], v[6:7] op_sel_hi:[0,1,1]
	v_cvt_pk_fp8_f32 v24, v1, v3
	v_med3_f32 v1, v6, s3, v75
	v_med3_f32 v3, v7, s3, v75
	v_cvt_pk_f32_fp8_sdwa v[6:7], v13 src0_sel:WORD_1
	v_cvt_pk_f32_fp8_e32 v[10:11], v13
	v_cvt_pk_f32_fp8_e32 v[12:13], v5
	v_cvt_pk_f32_fp8_sdwa v[4:5], v5 src0_sel:WORD_1
	v_pk_add_f32 v[6:7], v[6:7], 0 op_sel_hi:[1,0]
	v_pk_add_f32 v[10:11], v[10:11], 0 op_sel_hi:[1,0]
	v_cvt_pk_f32_fp8_e32 v[14:15], v9
	v_pk_add_f32 v[10:11], v[10:11], v[12:13]
	v_pk_add_f32 v[4:5], v[6:7], v[4:5]
	v_cvt_pk_f32_fp8_sdwa v[6:7], v17 src0_sel:WORD_1
	v_cvt_pk_f32_fp8_e32 v[12:13], v17
	v_cvt_pk_f32_fp8_sdwa v[8:9], v9 src0_sel:WORD_1
	v_cvt_pk_fp8_f32 v24, v1, v3 op_sel:[0,0,1]
	v_pk_add_f32 v[4:5], v[4:5], v[6:7]
	v_pk_add_f32 v[6:7], v[10:11], v[12:13]
	v_pk_add_f32 v[4:5], v[4:5], v[8:9]
	v_pk_add_f32 v[6:7], v[6:7], v[14:15]
	s_waitcnt vmcnt(0)
	v_pk_fma_f32 v[6:7], v[2:3], v[34:35], v[6:7] op_sel_hi:[0,1,1]
	v_med3_f32 v1, v6, s3, v75
	v_med3_f32 v3, v7, s3, v75
	v_cvt_pk_fp8_f32 v25, v1, v3
	v_pk_fma_f32 v[2:3], v[2:3], v[36:37], v[4:5] op_sel_hi:[0,1,1]
	v_med3_f32 v1, v2, s3, v75
	v_med3_f32 v2, v3, s3, v75
	v_cvt_pk_fp8_f32 v25, v1, v2 op_sel:[0,0,1]
	global_store_dwordx4 v50, v[22:25], s[10:11] sc1
